# baseline (speedup 1.0000x reference)
.Lp1b_3_x:
	v_mfma_f32_16x16x32_f16 v[136:139], v[64:67], v[116:119], 0
	v_mfma_f32_16x16x32_f16 v[140:143], v[68:71], v[116:119], 0
	v_cndmask_b32_e32 v158, 1, v158, vcc
	v_mfma_f32_16x16x32_f16 v[144:147], v[72:75], v[116:119], 0
	v_mfma_f32_16x16x32_f16 v[148:151], v[76:79], v[116:119], 0
	v_min3_i32 v160, v120, v121, v156
	v_min3_i32 v160, v122, v123, v160
	v_min3_i32 v160, v124, v125, v160
	v_min3_i32 v160, v126, v127, v160
	v_min3_i32 v160, v128, v129, v160
	v_min3_i32 v160, v130, v131, v160
	v_min3_i32 v160, v132, v133, v160
	v_min3_i32 v157, v134, v135, v160
	v_cmp_ge_i32_e32 vcc, v157, v156
	v_mfma_f32_16x16x32_f16 v[120:123], v[80:83], v[116:119], 0
	v_mfma_f32_16x16x32_f16 v[124:127], v[84:87], v[116:119], 0
	v_cndmask_b32_e32 v158, 2, v158, vcc
	v_mfma_f32_16x16x32_f16 v[128:131], v[88:91], v[116:119], 0
	v_mfma_f32_16x16x32_f16 v[132:135], v[92:95], v[116:119], 0
	v_min3_i32 v160, v136, v137, v157
	v_min3_i32 v160, v138, v139, v160
	v_min3_i32 v160, v140, v141, v160
	v_min3_i32 v160, v142, v143, v160
	v_min3_i32 v160, v144, v145, v160
	v_min3_i32 v160, v146, v147, v160
	v_min3_i32 v160, v148, v149, v160
	v_min3_i32 v156, v150, v151, v160
	v_cmp_ge_i32_e32 vcc, v156, v157
	v_mfma_f32_16x16x32_f16 v[136:139], v[96:99], v[116:119], 0
	v_mfma_f32_16x16x32_f16 v[140:143], v[100:103], v[116:119], 0
	v_cndmask_b32_e32 v158, 3, v158, vcc
	v_mfma_f32_16x16x32_f16 v[144:147], v[104:107], v[116:119], 0
	v_mfma_f32_16x16x32_f16 v[148:151], v[108:111], v[116:119], 0
	v_min3_i32 v160, v120, v121, v156
	v_min3_i32 v160, v122, v123, v160
	v_min3_i32 v160, v124, v125, v160
	v_min3_i32 v160, v126, v127, v160
	v_min3_i32 v160, v128, v129, v160
	v_min3_i32 v160, v130, v131, v160
	v_min3_i32 v160, v132, v133, v160
	v_min3_i32 v157, v134, v135, v160
	v_cmp_ge_i32_e32 vcc, v157, v156
	s_cmp_lt_u32 s50, 3
	s_cbranch_scc1 .Lit4a
	s_waitcnt vmcnt(0)
	s_branch .Lit4b

.Lit4b:
	global_load_dwordx4 v[116:119], v164, s[22:23] offset:1024
	v_mfma_f32_16x16x32_f16 v[120:123], v[16:19], v[112:115], 0
	v_mfma_f32_16x16x32_f16 v[124:127], v[20:23], v[112:115], 0
	v_cndmask_b32_e32 v158, 4, v158, vcc
	v_mfma_f32_16x16x32_f16 v[128:131], v[24:27], v[112:115], 0
	v_mfma_f32_16x16x32_f16 v[132:135], v[28:31], v[112:115], 0
	v_min3_i32 v160, v136, v137, v157
	v_min3_i32 v160, v138, v139, v160
	v_min3_i32 v160, v140, v141, v160
	v_min3_i32 v160, v142, v143, v160
	v_min3_i32 v160, v144, v145, v160
	v_min3_i32 v160, v146, v147, v160
	v_min3_i32 v160, v148, v149, v160
	v_min3_i32 v156, v150, v151, v160
	v_cmp_ge_i32_e32 vcc, v156, v157
	v_mfma_f32_16x16x32_f16 v[136:139], v[32:35], v[112:115], 0
	v_mfma_f32_16x16x32_f16 v[140:143], v[36:39], v[112:115], 0
	v_cndmask_b32_e32 v158, 5, v158, vcc
	v_add_u32_e32 v162, s40, v158
	v_lshl_or_b32 v162, v162, 2, v166
	v_mov_b32_e32 v163, v156
	ds_min_u64 v167, v[162:163] offset:16768
	v_mfma_f32_16x16x32_f16 v[144:147], v[40:43], v[112:115], 0
	v_mfma_f32_16x16x32_f16 v[148:151], v[44:47], v[112:115], 0
	v_min3_i32 v160, v120, v121, s41
	v_min3_i32 v160, v122, v123, v160
	v_min3_i32 v160, v124, v125, v160
	v_min3_i32 v160, v126, v127, v160
	v_min3_i32 v160, v128, v129, v160
	v_min3_i32 v160, v130, v131, v160
	v_min3_i32 v160, v132, v133, v160
	v_min3_i32 v157, v134, v135, v160
	v_mfma_f32_16x16x32_f16 v[120:123], v[48:51], v[112:115], 0
	v_mfma_f32_16x16x32_f16 v[124:127], v[52:55], v[112:115], 0
	v_mov_b32_e32 v158, 0
	v_mfma_f32_16x16x32_f16 v[128:131], v[56:59], v[112:115], 0
	v_mfma_f32_16x16x32_f16 v[132:135], v[60:63], v[112:115], 0
	v_min3_i32 v160, v136, v137, v157
	v_min3_i32 v160, v138, v139, v160
	v_min3_i32 v160, v140, v141, v160
	v_min3_i32 v160, v142, v143, v160
	v_min3_i32 v160, v144, v145, v160
	v_min3_i32 v160, v146, v147, v160
	v_min3_i32 v160, v148, v149, v160
	v_min3_i32 v156, v150, v151, v160
	v_cmp_ge_i32_e32 vcc, v156, v157
	v_mfma_f32_16x16x32_f16 v[136:139], v[64:67], v[112:115], 0
	v_mfma_f32_16x16x32_f16 v[140:143], v[68:71], v[112:115], 0
	v_cndmask_b32_e32 v158, 1, v158, vcc
	v_mfma_f32_16x16x32_f16 v[144:147], v[72:75], v[112:115], 0
	v_mfma_f32_16x16x32_f16 v[148:151], v[76:79], v[112:115], 0
	v_min3_i32 v160, v120, v121, v156
	v_min3_i32 v160, v122, v123, v160
	v_min3_i32 v160, v124, v125, v160
	v_min3_i32 v160, v126, v127, v160
	v_min3_i32 v160, v128, v129, v160
	v_min3_i32 v160, v130, v131, v160
	v_min3_i32 v160, v132, v133, v160
	v_min3_i32 v157, v134, v135, v160
	v_cmp_ge_i32_e32 vcc, v157, v156
	v_mfma_f32_16x16x32_f16 v[120:123], v[80:83], v[112:115], 0
	v_mfma_f32_16x16x32_f16 v[124:127], v[84:87], v[112:115], 0
	v_cndmask_b32_e32 v158, 2, v158, vcc
	v_mfma_f32_16x16x32_f16 v[128:131], v[88:91], v[112:115], 0
	v_mfma_f32_16x16x32_f16 v[132:135], v[92:95], v[112:115], 0
	v_min3_i32 v160, v136, v137, v157
	v_min3_i32 v160, v138, v139, v160
	v_min3_i32 v160, v140, v141, v160
	v_min3_i32 v160, v142, v143, v160
	v_min3_i32 v160, v144, v145, v160
	v_min3_i32 v160, v146, v147, v160
	v_min3_i32 v160, v148, v149, v160
	v_min3_i32 v156, v150, v151, v160
	v_cmp_ge_i32_e32 vcc, v156, v157
	v_mfma_f32_16x16x32_f16 v[136:139], v[96:99], v[112:115], 0
	v_mfma_f32_16x16x32_f16 v[140:143], v[100:103], v[112:115], 0
	v_cndmask_b32_e32 v158, 3, v158, vcc
	v_mfma_f32_16x16x32_f16 v[144:147], v[104:107], v[112:115], 0
	v_mfma_f32_16x16x32_f16 v[148:151], v[108:111], v[112:115], 0
	v_min3_i32 v160, v120, v121, v156
	v_min3_i32 v160, v122, v123, v160
	v_min3_i32 v160, v124, v125, v160
	v_min3_i32 v160, v126, v127, v160
	v_min3_i32 v160, v128, v129, v160
	v_min3_i32 v160, v130, v131, v160
	v_min3_i32 v160, v132, v133, v160
	v_min3_i32 v157, v134, v135, v160
	v_cmp_ge_i32_e32 vcc, v157, v156
	s_waitcnt vmcnt(0)
	global_load_dwordx4 v[112:115], v164, s[22:23] offset:2048
	v_mfma_f32_16x16x32_f16 v[120:123], v[16:19], v[116:119], 0
	v_mfma_f32_16x16x32_f16 v[124:127], v[20:23], v[116:119], 0
	v_cndmask_b32_e32 v158, 4, v158, vcc
	v_mfma_f32_16x16x32_f16 v[128:131], v[24:27], v[116:119], 0
	v_mfma_f32_16x16x32_f16 v[132:135], v[28:31], v[116:119], 0
	v_min3_i32 v160, v136, v137, v157
	v_min3_i32 v160, v138, v139, v160
	v_min3_i32 v160, v140, v141, v160
	v_min3_i32 v160, v142, v143, v160
	v_min3_i32 v160, v144, v145, v160
	v_min3_i32 v160, v146, v147, v160
	v_min3_i32 v160, v148, v149, v160
	v_min3_i32 v156, v150, v151, v160
	v_cmp_ge_i32_e32 vcc, v156, v157
	v_mfma_f32_16x16x32_f16 v[136:139], v[32:35], v[116:119], 0
	v_mfma_f32_16x16x32_f16 v[140:143], v[36:39], v[116:119], 0
	v_cndmask_b32_e32 v158, 5, v158, vcc
	v_add_u32_e32 v162, s40, v158
	v_lshl_or_b32 v162, v162, 2, v166
	v_mov_b32_e32 v163, v156
	ds_min_u64 v167, v[162:163] offset:16896
	v_mfma_f32_16x16x32_f16 v[144:147], v[40:43], v[116:119], 0
	v_mfma_f32_16x16x32_f16 v[148:151], v[44:47], v[116:119], 0
	v_min3_i32 v160, v120, v121, s41
	v_min3_i32 v160, v122, v123, v160
	v_min3_i32 v160, v124, v125, v160
	v_min3_i32 v160, v126, v127, v160
	v_min3_i32 v160, v128, v129, v160
	v_min3_i32 v160, v130, v131, v160
	v_min3_i32 v160, v132, v133, v160
	v_min3_i32 v157, v134, v135, v160
	v_mfma_f32_16x16x32_f16 v[120:123], v[48:51], v[116:119], 0
	v_mfma_f32_16x16x32_f16 v[124:127], v[52:55], v[116:119], 0
	v_mov_b32_e32 v158, 0
	v_mfma_f32_16x16x32_f16 v[128:131], v[56:59], v[116:119], 0
	v_mfma_f32_16x16x32_f16 v[132:135], v[60:63], v[116:119], 0
	v_min3_i32 v160, v136, v137, v157
	v_min3_i32 v160, v138, v139, v160
	v_min3_i32 v160, v140, v141, v160
	v_min3_i32 v160, v142, v143, v160
	v_min3_i32 v160, v144, v145, v160
	v_min3_i32 v160, v146, v147, v160
	v_min3_i32 v160, v148, v149, v160
	v_min3_i32 v156, v150, v151, v160
	v_cmp_ge_i32_e32 vcc, v156, v157
	v_mfma_f32_16x16x32_f16 v[136:139], v[64:67], v[116:119], 0
	v_mfma_f32_16x16x32_f16 v[140:143], v[68:71], v[116:119], 0
	v_cndmask_b32_e32 v158, 1, v158, vcc
	v_mfma_f32_16x16x32_f16 v[144:147], v[72:75], v[116:119], 0
	v_mfma_f32_16x16x32_f16 v[148:151], v[76:79], v[116:119], 0
	v_min3_i32 v160, v120, v121, v156
	v_min3_i32 v160, v122, v123, v160
	v_min3_i32 v160, v124, v125, v160
	v_min3_i32 v160, v126, v127, v160
	v_min3_i32 v160, v128, v129, v160
	v_min3_i32 v160, v130, v131, v160
	v_min3_i32 v160, v132, v133, v160
	v_min3_i32 v157, v134, v135, v160
	v_cmp_ge_i32_e32 vcc, v157, v156
	v_mfma_f32_16x16x32_f16 v[120:123], v[80:83], v[116:119], 0
	v_mfma_f32_16x16x32_f16 v[124:127], v[84:87], v[116:119], 0
	v_cndmask_b32_e32 v158, 2, v158, vcc
	v_mfma_f32_16x16x32_f16 v[128:131], v[88:91], v[116:119], 0
	v_mfma_f32_16x16x32_f16 v[132:135], v[92:95], v[116:119], 0
	v_min3_i32 v160, v136, v137, v157
	v_min3_i32 v160, v138, v139, v160
	v_min3_i32 v160, v140, v141, v160
	v_min3_i32 v160, v142, v143, v160
	v_min3_i32 v160, v144, v145, v160
	v_min3_i32 v160, v146, v147, v160
	v_min3_i32 v160, v148, v149, v160
	v_min3_i32 v156, v150, v151, v160
	v_cmp_ge_i32_e32 vcc, v156, v157
	v_mfma_f32_16x16x32_f16 v[136:139], v[96:99], v[116:119], 0
	v_mfma_f32_16x16x32_f16 v[140:143], v[100:103], v[116:119], 0
	v_cndmask_b32_e32 v158, 3, v158, vcc
	v_mfma_f32_16x16x32_f16 v[144:147], v[104:107], v[116:119], 0
	v_mfma_f32_16x16x32_f16 v[148:151], v[108:111], v[116:119], 0
	v_min3_i32 v160, v120, v121, v156
	v_min3_i32 v160, v122, v123, v160
	v_min3_i32 v160, v124, v125, v160
	v_min3_i32 v160, v126, v127, v160
	v_min3_i32 v160, v128, v129, v160
	v_min3_i32 v160, v130, v131, v160
	v_min3_i32 v160, v132, v133, v160
	v_min3_i32 v157, v134, v135, v160
	v_cmp_ge_i32_e32 vcc, v157, v156
	s_waitcnt vmcnt(0)
	global_load_dwordx4 v[116:119], v164, s[22:23] offset:3072
	v_mfma_f32_16x16x32_f16 v[120:123], v[16:19], v[112:115], 0
	v_mfma_f32_16x16x32_f16 v[124:127], v[20:23], v[112:115], 0
	v_cndmask_b32_e32 v158, 4, v158, vcc
	v_mfma_f32_16x16x32_f16 v[128:131], v[24:27], v[112:115], 0
	v_mfma_f32_16x16x32_f16 v[132:135], v[28:31], v[112:115], 0
	v_min3_i32 v160, v136, v137, v157
	v_min3_i32 v160, v138, v139, v160
	v_min3_i32 v160, v140, v141, v160
	v_min3_i32 v160, v142, v143, v160
	v_min3_i32 v160, v144, v145, v160
	v_min3_i32 v160, v146, v147, v160
	v_min3_i32 v160, v148, v149, v160
	v_min3_i32 v156, v150, v151, v160
	v_cmp_ge_i32_e32 vcc, v156, v157
	v_mfma_f32_16x16x32_f16 v[136:139], v[32:35], v[112:115], 0
	v_mfma_f32_16x16x32_f16 v[140:143], v[36:39], v[112:115], 0
	v_cndmask_b32_e32 v158, 5, v158, vcc
	v_add_u32_e32 v162, s40, v158
	v_lshl_or_b32 v162, v162, 2, v166
	v_mov_b32_e32 v163, v156
	ds_min_u64 v167, v[162:163] offset:17024
	v_mfma_f32_16x16x32_f16 v[144:147], v[40:43], v[112:115], 0
	v_mfma_f32_16x16x32_f16 v[148:151], v[44:47], v[112:115], 0
	v_min3_i32 v160, v120, v121, s41
	v_min3_i32 v160, v122, v123, v160
	v_min3_i32 v160, v124, v125, v160
	v_min3_i32 v160, v126, v127, v160
	v_min3_i32 v160, v128, v129, v160
	v_min3_i32 v160, v130, v131, v160
	v_min3_i32 v160, v132, v133, v160
	v_min3_i32 v157, v134, v135, v160
	s_waitcnt lgkmcnt(0)
	s_barrier
	s_cmp_eq_u32 s50, 3
	s_cbranch_scc0 .Lp1a_6_x
	s_lshl_b32 s60, s50, 7
	v_add_u32_e32 v2, s60, v169
	ds_read_b32 v178, v2 offset:16384
	s_lshl_b32 s60, s50, 4
	v_add_u32_e32 v2, s60, v177
	v_mul_u32_u24_e32 v3, 0x556, v2
	v_lshrrev_b32_e32 v3, 16, v3
	v_mul_u32_u24_e32 v4, 48, v3
	v_sub_u32_e32 v4, v2, v4
	v_mul_u32_u24_e32 v3, 0x6c0, v3
	v_mad_u32_u24 v215, v4, 12, v3
	v_add_u32_e32 v215, v215, v175
	s_lshl_b32 s60, s50, 10
	v_add_u32_e32 v210, s60, v170

.Lp1b_6_y:
	v_mfma_f32_16x16x32_f16 v[136:139], v[64:67], v[112:115], 0
	v_mfma_f32_16x16x32_f16 v[140:143], v[68:71], v[112:115], 0
	v_cndmask_b32_e32 v158, 1, v158, vcc
	v_mfma_f32_16x16x32_f16 v[144:147], v[72:75], v[112:115], 0
	v_mfma_f32_16x16x32_f16 v[148:151], v[76:79], v[112:115], 0
	v_min3_i32 v160, v120, v121, v156
	v_min3_i32 v160, v122, v123, v160
	v_min3_i32 v160, v124, v125, v160
	v_min3_i32 v160, v126, v127, v160
	v_min3_i32 v160, v128, v129, v160
	v_min3_i32 v160, v130, v131, v160
	v_min3_i32 v160, v132, v133, v160
	v_min3_i32 v157, v134, v135, v160
	v_cmp_ge_i32_e32 vcc, v157, v156
	v_mfma_f32_16x16x32_f16 v[120:123], v[80:83], v[112:115], 0
	v_mfma_f32_16x16x32_f16 v[124:127], v[84:87], v[112:115], 0
	v_cndmask_b32_e32 v158, 2, v158, vcc
	v_mfma_f32_16x16x32_f16 v[128:131], v[88:91], v[112:115], 0
	v_mfma_f32_16x16x32_f16 v[132:135], v[92:95], v[112:115], 0
	v_min3_i32 v160, v136, v137, v157
	v_min3_i32 v160, v138, v139, v160
	v_min3_i32 v160, v140, v141, v160
	v_min3_i32 v160, v142, v143, v160
	v_min3_i32 v160, v144, v145, v160
	v_min3_i32 v160, v146, v147, v160
	v_min3_i32 v160, v148, v149, v160
	v_min3_i32 v156, v150, v151, v160
	v_cmp_ge_i32_e32 vcc, v156, v157
	v_mfma_f32_16x16x32_f16 v[136:139], v[96:99], v[112:115], 0
	v_mfma_f32_16x16x32_f16 v[140:143], v[100:103], v[112:115], 0
	v_cndmask_b32_e32 v158, 3, v158, vcc
	v_mfma_f32_16x16x32_f16 v[144:147], v[104:107], v[112:115], 0
	v_mfma_f32_16x16x32_f16 v[148:151], v[108:111], v[112:115], 0
	v_min3_i32 v160, v120, v121, v156
	v_min3_i32 v160, v122, v123, v160
	v_min3_i32 v160, v124, v125, v160
	v_min3_i32 v160, v126, v127, v160
	v_min3_i32 v160, v128, v129, v160
	v_min3_i32 v160, v130, v131, v160
	v_min3_i32 v160, v132, v133, v160
	v_min3_i32 v157, v134, v135, v160
	v_cmp_ge_i32_e32 vcc, v157, v156
	s_cmp_lg_u32 s50, 2
	s_cbranch_scc1 .Lit7a
	s_waitcnt vmcnt(0)
	s_branch .Lit7b

.Lit7b:
	global_load_dwordx4 v[112:115], v164, s[24:25]
	v_mfma_f32_16x16x32_f16 v[120:123], v[16:19], v[116:119], 0
	v_mfma_f32_16x16x32_f16 v[124:127], v[20:23], v[116:119], 0
	v_cndmask_b32_e32 v158, 4, v158, vcc
	v_mfma_f32_16x16x32_f16 v[128:131], v[24:27], v[116:119], 0
	v_mfma_f32_16x16x32_f16 v[132:135], v[28:31], v[116:119], 0
	v_min3_i32 v160, v136, v137, v157
	v_min3_i32 v160, v138, v139, v160
	v_min3_i32 v160, v140, v141, v160
	v_min3_i32 v160, v142, v143, v160
	v_min3_i32 v160, v144, v145, v160
	v_min3_i32 v160, v146, v147, v160
	v_min3_i32 v160, v148, v149, v160
	v_min3_i32 v156, v150, v151, v160
	v_cmp_ge_i32_e32 vcc, v156, v157
	v_mfma_f32_16x16x32_f16 v[136:139], v[32:35], v[116:119], 0
	v_mfma_f32_16x16x32_f16 v[140:143], v[36:39], v[116:119], 0
	v_cndmask_b32_e32 v158, 5, v158, vcc
	v_add_u32_e32 v162, s40, v158
	v_lshl_or_b32 v162, v162, 2, v166
	v_mov_b32_e32 v163, v156
	ds_min_u64 v167, v[162:163] offset:17152
	v_mfma_f32_16x16x32_f16 v[144:147], v[40:43], v[116:119], 0
	v_mfma_f32_16x16x32_f16 v[148:151], v[44:47], v[116:119], 0
	v_min3_i32 v160, v120, v121, s41
	v_min3_i32 v160, v122, v123, v160
	v_min3_i32 v160, v124, v125, v160
	v_min3_i32 v160, v126, v127, v160
	v_min3_i32 v160, v128, v129, v160
	v_min3_i32 v160, v130, v131, v160
	v_min3_i32 v160, v132, v133, v160
	v_min3_i32 v157, v134, v135, v160
	v_mfma_f32_16x16x32_f16 v[120:123], v[48:51], v[116:119], 0
	v_mfma_f32_16x16x32_f16 v[124:127], v[52:55], v[116:119], 0
	v_mov_b32_e32 v158, 0
	v_mfma_f32_16x16x32_f16 v[128:131], v[56:59], v[116:119], 0
	v_mfma_f32_16x16x32_f16 v[132:135], v[60:63], v[116:119], 0
	v_min3_i32 v160, v136, v137, v157
	v_min3_i32 v160, v138, v139, v160
	v_min3_i32 v160, v140, v141, v160
	v_min3_i32 v160, v142, v143, v160
	v_min3_i32 v160, v144, v145, v160
	v_min3_i32 v160, v146, v147, v160
	v_min3_i32 v160, v148, v149, v160
	v_min3_i32 v156, v150, v151, v160
	v_cmp_ge_i32_e32 vcc, v156, v157
	v_mfma_f32_16x16x32_f16 v[136:139], v[64:67], v[116:119], 0
	v_mfma_f32_16x16x32_f16 v[140:143], v[68:71], v[116:119], 0
	v_cndmask_b32_e32 v158, 1, v158, vcc
	v_mfma_f32_16x16x32_f16 v[144:147], v[72:75], v[116:119], 0
	v_mfma_f32_16x16x32_f16 v[148:151], v[76:79], v[116:119], 0
	v_min3_i32 v160, v120, v121, v156
	v_min3_i32 v160, v122, v123, v160
	v_min3_i32 v160, v124, v125, v160
	v_min3_i32 v160, v126, v127, v160
	v_min3_i32 v160, v128, v129, v160
	v_min3_i32 v160, v130, v131, v160
	v_min3_i32 v160, v132, v133, v160
	v_min3_i32 v157, v134, v135, v160
	v_cmp_ge_i32_e32 vcc, v157, v156
	v_mfma_f32_16x16x32_f16 v[120:123], v[80:83], v[116:119], 0
	v_mfma_f32_16x16x32_f16 v[124:127], v[84:87], v[116:119], 0
	v_cndmask_b32_e32 v158, 2, v158, vcc
	v_mfma_f32_16x16x32_f16 v[128:131], v[88:91], v[116:119], 0
	v_mfma_f32_16x16x32_f16 v[132:135], v[92:95], v[116:119], 0
	v_min3_i32 v160, v136, v137, v157
	v_min3_i32 v160, v138, v139, v160
	v_min3_i32 v160, v140, v141, v160
	v_min3_i32 v160, v142, v143, v160
	v_min3_i32 v160, v144, v145, v160
	v_min3_i32 v160, v146, v147, v160
	v_min3_i32 v160, v148, v149, v160
	v_min3_i32 v156, v150, v151, v160
	v_cmp_ge_i32_e32 vcc, v156, v157
	v_mfma_f32_16x16x32_f16 v[136:139], v[96:99], v[116:119], 0
	v_mfma_f32_16x16x32_f16 v[140:143], v[100:103], v[116:119], 0
	v_cndmask_b32_e32 v158, 3, v158, vcc
	v_mfma_f32_16x16x32_f16 v[144:147], v[104:107], v[116:119], 0
	v_mfma_f32_16x16x32_f16 v[148:151], v[108:111], v[116:119], 0
	v_min3_i32 v160, v120, v121, v156
	v_min3_i32 v160, v122, v123, v160
	v_min3_i32 v160, v124, v125, v160
	v_min3_i32 v160, v126, v127, v160
	v_min3_i32 v160, v128, v129, v160
	v_min3_i32 v160, v130, v131, v160
	v_min3_i32 v160, v132, v133, v160
	v_min3_i32 v157, v134, v135, v160
	v_cmp_ge_i32_e32 vcc, v157, v156
	s_waitcnt vmcnt(0)
	v_mfma_f32_16x16x32_f16 v[120:123], v[16:19], v[112:115], 0
	v_mfma_f32_16x16x32_f16 v[124:127], v[20:23], v[112:115], 0
	v_cndmask_b32_e32 v158, 4, v158, vcc
	v_mfma_f32_16x16x32_f16 v[128:131], v[24:27], v[112:115], 0
	v_mfma_f32_16x16x32_f16 v[132:135], v[28:31], v[112:115], 0
	v_min3_i32 v160, v136, v137, v157
	v_min3_i32 v160, v138, v139, v160
	v_min3_i32 v160, v140, v141, v160
	v_min3_i32 v160, v142, v143, v160
	v_min3_i32 v160, v144, v145, v160
	v_min3_i32 v160, v146, v147, v160
	v_min3_i32 v160, v148, v149, v160
	v_min3_i32 v156, v150, v151, v160
	v_cmp_ge_i32_e32 vcc, v156, v157
	v_mfma_f32_16x16x32_f16 v[136:139], v[32:35], v[112:115], 0
	v_mfma_f32_16x16x32_f16 v[140:143], v[36:39], v[112:115], 0
	v_cndmask_b32_e32 v158, 5, v158, vcc
	v_add_u32_e32 v162, s40, v158
	v_lshl_or_b32 v162, v162, 2, v166
	v_mov_b32_e32 v163, v156
	ds_min_u64 v167, v[162:163] offset:17280
	v_mfma_f32_16x16x32_f16 v[144:147], v[40:43], v[112:115], 0
	v_mfma_f32_16x16x32_f16 v[148:151], v[44:47], v[112:115], 0
	v_min3_i32 v160, v120, v121, s41
	v_min3_i32 v160, v122, v123, v160
	v_min3_i32 v160, v124, v125, v160
	v_min3_i32 v160, v126, v127, v160
	v_min3_i32 v160, v128, v129, v160
	v_min3_i32 v160, v130, v131, v160
	v_min3_i32 v160, v132, v133, v160
	v_min3_i32 v157, v134, v135, v160
	v_mfma_f32_16x16x32_f16 v[120:123], v[48:51], v[112:115], 0
	v_mfma_f32_16x16x32_f16 v[124:127], v[52:55], v[112:115], 0
	v_mov_b32_e32 v158, 0
	v_mfma_f32_16x16x32_f16 v[128:131], v[56:59], v[112:115], 0
	v_mfma_f32_16x16x32_f16 v[132:135], v[60:63], v[112:115], 0
	v_min3_i32 v160, v136, v137, v157
	v_min3_i32 v160, v138, v139, v160
	v_min3_i32 v160, v140, v141, v160
	v_min3_i32 v160, v142, v143, v160
	v_min3_i32 v160, v144, v145, v160
	v_min3_i32 v160, v146, v147, v160
	v_min3_i32 v160, v148, v149, v160
	v_min3_i32 v156, v150, v151, v160
	v_cmp_ge_i32_e32 vcc, v156, v157
	v_mfma_f32_16x16x32_f16 v[136:139], v[64:67], v[112:115], 0
	v_mfma_f32_16x16x32_f16 v[140:143], v[68:71], v[112:115], 0
	v_cndmask_b32_e32 v158, 1, v158, vcc
	v_mfma_f32_16x16x32_f16 v[144:147], v[72:75], v[112:115], 0
	v_mfma_f32_16x16x32_f16 v[148:151], v[76:79], v[112:115], 0
	v_min3_i32 v160, v120, v121, v156
	v_min3_i32 v160, v122, v123, v160
	v_min3_i32 v160, v124, v125, v160
	v_min3_i32 v160, v126, v127, v160
	v_min3_i32 v160, v128, v129, v160
	v_min3_i32 v160, v130, v131, v160
	v_min3_i32 v160, v132, v133, v160
	v_min3_i32 v157, v134, v135, v160
	v_cmp_ge_i32_e32 vcc, v157, v156
	v_mfma_f32_16x16x32_f16 v[120:123], v[80:83], v[112:115], 0
	v_mfma_f32_16x16x32_f16 v[124:127], v[84:87], v[112:115], 0
	v_cndmask_b32_e32 v158, 2, v158, vcc
	v_mfma_f32_16x16x32_f16 v[128:131], v[88:91], v[112:115], 0
	v_mfma_f32_16x16x32_f16 v[132:135], v[92:95], v[112:115], 0
	v_min3_i32 v160, v136, v137, v157
	v_min3_i32 v160, v138, v139, v160
	v_min3_i32 v160, v140, v141, v160
	v_min3_i32 v160, v142, v143, v160
	v_min3_i32 v160, v144, v145, v160
	v_min3_i32 v160, v146, v147, v160
	v_min3_i32 v160, v148, v149, v160
	v_min3_i32 v156, v150, v151, v160
	v_cmp_ge_i32_e32 vcc, v156, v157
	v_mfma_f32_16x16x32_f16 v[136:139], v[96:99], v[112:115], 0
	v_mfma_f32_16x16x32_f16 v[140:143], v[100:103], v[112:115], 0
	v_cndmask_b32_e32 v158, 3, v158, vcc
	v_mfma_f32_16x16x32_f16 v[144:147], v[104:107], v[112:115], 0
	v_mfma_f32_16x16x32_f16 v[148:151], v[108:111], v[112:115], 0
	v_min3_i32 v160, v120, v121, v156
	v_min3_i32 v160, v122, v123, v160
	v_min3_i32 v160, v124, v125, v160
	v_min3_i32 v160, v126, v127, v160
	v_min3_i32 v160, v128, v129, v160
	v_min3_i32 v160, v130, v131, v160
	v_min3_i32 v160, v132, v133, v160
	v_min3_i32 v157, v134, v135, v160
	v_cmp_ge_i32_e32 vcc, v157, v156
	s_nop 1
	v_cndmask_b32_e32 v158, 4, v158, vcc
	s_nop 7
	v_min3_i32 v160, v136, v137, v157
	v_min3_i32 v160, v138, v139, v160
	v_min3_i32 v160, v140, v141, v160
	v_min3_i32 v160, v142, v143, v160
	v_min3_i32 v160, v144, v145, v160
	v_min3_i32 v160, v146, v147, v160
	v_min3_i32 v160, v148, v149, v160
	v_min3_i32 v156, v150, v151, v160
	v_cmp_ge_i32_e32 vcc, v156, v157
	s_nop 1
	v_cndmask_b32_e32 v158, 5, v158, vcc
	v_add_u32_e32 v162, s40, v158
	v_lshl_or_b32 v162, v162, 2, v166
	v_mov_b32_e32 v163, v156
	ds_min_u64 v167, v[162:163] offset:17408
	s_waitcnt lgkmcnt(0)
	s_barrier
	s_add_i32 s65, s50, 4
	s_mov_b32 s66, 8
	s_cmp_ge_u32 s50, 2
	s_cbranch_scc0 .Lq1
	s_lshl_b32 s60, s65, 7
	v_add_u32_e32 v2, s60, v169
	ds_read_b32 v216, v2 offset:16384
	s_lshl_b32 s60, s65, 4
	v_add_u32_e32 v2, s60, v177
	v_mul_u32_u24_e32 v3, 0x556, v2
	v_lshrrev_b32_e32 v3, 16, v3
	v_mul_u32_u24_e32 v4, 48, v3
	v_sub_u32_e32 v4, v2, v4
	v_mul_u32_u24_e32 v3, 0x6c0, v3
	v_mad_u32_u24 v253, v4, 12, v3
	v_add_u32_e32 v253, v253, v175
	s_lshl_b32 s60, s65, 10
	v_add_u32_e32 v248, s60, v170
